# speedup vs baseline: 1.0009x; 1.0009x over previous
_Z12oproj_kernelPKDF16_S0_PKfPf:
	s_load_dwordx8 s[4:11], s[0:1], 0x0
	s_lshl_b32 s0, s2, 2
	s_lshr_b32 s1, s2, 6
	s_and_b32 s0, s0, 28
	s_add_i32 s0, s0, s1
	v_bfe_u32 v14, v0, 6, 1
	s_bfe_u32 s13, s2, 0x30003
	s_lshl_b32 s12, s0, 7
	s_mul_i32 s0, s0, 0x44000
	v_bfe_u32 v12, v0, 4, 2
	v_and_b32_e32 v1, 7, v0
	v_lshlrev_b32_e32 v2, 2, v14
	s_mul_hi_i32 s1, s12, 0x880
	s_waitcnt lgkmcnt(0)
	s_add_u32 s0, s4, s0
	v_lshrrev_b32_e32 v13, 6, v0
	v_bitop3_b32 v1, v2, v1, v12 bitop3:0x36
	v_bfe_u32 v2, v0, 3, 3
	s_addc_u32 s1, s5, s1
	s_mul_i32 s2, s13, 0x44000
	v_lshl_or_b32 v2, v13, 3, v2
	s_add_u32 s2, s6, s2
	v_mul_u32_u24_e32 v2, 0x440, v2
	s_addc_u32 s3, s7, 0
	v_lshlrev_b32_e32 v2, 1, v2
	v_mov_b32_e32 v3, 0
	v_lshl_add_u64 v[4:5], s[0:1], 0, v[2:3]
	v_lshl_add_u64 v[10:11], s[2:3], 0, v[2:3]
	v_bfe_u32 v2, v0, 1, 3
	v_and_b32_e32 v9, 15, v0
	v_lshlrev_b32_e32 v6, 4, v1
	v_mov_b32_e32 v7, v3
	v_xor_b32_e32 v17, v12, v2
	v_bitop3_b32 v38, v12, v2, 4 bitop3:0x36
	v_lshlrev_b32_e32 v2, 10, v13
	v_lshl_add_u64 v[4:5], v[4:5], 0, v[6:7]
	v_lshl_add_u64 v[6:7], v[10:11], 0, v[6:7]
	v_lshlrev_b32_e32 v10, 7, v9
	v_add_u32_e32 v94, 0, v2
	s_mov_b64 s[0:1], 0x22000
	s_mov_b64 s[14:15], src_shared_base
	v_lshl_or_b32 v62, v14, 13, v10
	v_lshl_add_u64 v[10:11], v[4:5], 0, s[0:1]
	v_lshl_add_u64 v[12:13], v[6:7], 0, s[0:1]
	v_readfirstlane_b32 s22, v94
	s_mov_b32 s0, m0
	s_mov_b32 m0, s22
	s_nop 0
	global_load_lds_dwordx4 v[4:5], off
	s_mov_b32 m0, s0
	v_mov_b32_e32 v95, s15
	s_mov_b64 s[0:1], 0x4000
	v_lshl_add_u64 v[14:15], v[94:95], 0, s[0:1]
	v_lshrrev_b32_e32 v1, 2, v0
	v_readfirstlane_b32 s23, v14
	s_mov_b32 s2, m0
	s_mov_b32 m0, s23
	s_nop 0
	global_load_lds_dwordx4 v[6:7], off
	s_mov_b32 m0, s2
	s_mov_b64 s[2:3], 0x2000
	v_lshl_add_u64 v[14:15], v[94:95], 0, s[2:3]
	v_and_b32_e32 v8, 0x60, v1
	v_readfirstlane_b32 s20, v14
	s_mov_b32 s4, m0
	s_mov_b32 m0, s20
	s_nop 0
	global_load_lds_dwordx4 v[10:11], off
	s_mov_b32 m0, s4
	s_mov_b64 s[4:5], 0x6000
	v_lshl_add_u64 v[10:11], v[94:95], 0, s[4:5]
	v_mov_b32_e32 v11, s15
	v_readfirstlane_b32 s21, v10
	s_mov_b32 s6, m0
	s_mov_b32 m0, s21
	s_nop 0
	global_load_lds_dwordx4 v[12:13], off
	s_mov_b32 m0, s6
	v_add_u32_e32 v10, 0x8000, v94
	s_mov_b64 s[6:7], 0x80
	v_lshl_add_u64 v[12:13], v[4:5], 0, s[6:7]
	v_readfirstlane_b32 s16, v10
	s_mov_b32 s14, m0
	s_mov_b32 m0, s16
	s_nop 0
	global_load_lds_dwordx4 v[12:13], off
	s_mov_b32 m0, s14
	v_lshl_add_u64 v[14:15], v[10:11], 0, s[0:1]
	v_lshl_add_u64 v[12:13], v[6:7], 0, s[6:7]
	v_readfirstlane_b32 s18, v14
	s_mov_b32 s6, m0
	s_mov_b32 m0, s18
	s_nop 0
	global_load_lds_dwordx4 v[12:13], off
	s_mov_b32 m0, s6
	s_mov_b64 s[14:15], 0x22080
	v_lshl_add_u64 v[14:15], v[10:11], 0, s[2:3]
	v_lshl_add_u64 v[12:13], v[4:5], 0, s[14:15]
	v_readfirstlane_b32 s6, v14
	s_mov_b32 s7, m0
	s_mov_b32 m0, s6
	s_nop 0
	global_load_lds_dwordx4 v[12:13], off
	s_mov_b32 m0, s7
	v_lshl_add_u64 v[10:11], v[10:11], 0, s[4:5]
	s_add_i32 s26, 0, 0x10000
	v_or_b32_e32 v16, v8, v9
	v_lshl_add_u64 v[12:13], v[6:7], 0, s[14:15]
	v_readfirstlane_b32 s14, v10
	s_mov_b32 s7, m0
	s_mov_b32 m0, s14
	s_nop 0
	global_load_lds_dwordx4 v[12:13], off
	s_mov_b32 m0, s7
	v_add_u32_e32 v10, s26, v2
	v_mov_b32_e32 v11, v95
	s_mov_b64 s[24:25], 0x100
	v_lshlrev_b32_e32 v102, 7, v16
	v_lshl_add_u64 v[12:13], v[4:5], 0, s[24:25]
	v_readfirstlane_b32 s7, v10
	v_lshl_add_u64 v[10:11], v[10:11], 0, s[0:1]
	v_lshlrev_b32_e32 v103, 4, v17
	s_mov_b32 s15, m0
	s_mov_b32 m0, s7
	s_nop 0
	global_load_lds_dwordx4 v[12:13], off
	s_mov_b32 m0, s15
	v_lshl_add_u64 v[12:13], v[6:7], 0, s[24:25]
	v_add_u32_e32 v11, 0, v102
	v_add_u32_e32 v46, 0, v62
	v_add_u32_e32 v106, 0x10000, v94
	v_mov_b32_e32 v107, v95
	s_mov_b64 s[24:25], 0x22100
	v_readfirstlane_b32 s7, v10
	s_mov_b32 s15, m0
	s_mov_b32 m0, s7
	s_nop 0
	global_load_lds_dwordx4 v[12:13], off
	s_mov_b32 m0, s15
	v_add_u32_e32 v2, v11, v103
	v_add_u32_e32 v10, v46, v103
	v_lshlrev_b32_e32 v104, 4, v38
	v_lshl_add_u64 v[12:13], v[4:5], 0, s[24:25]
	v_lshl_add_u64 v[38:39], v[106:107], 0, s[2:3]
	s_waitcnt vmcnt(6)
	s_barrier
	ds_read_b128 v[14:17], v2
	ds_read_b128 v[18:21], v2 offset:2048
	ds_read_b128 v[22:25], v10 offset:16384
	ds_read_b128 v[26:29], v10 offset:18432
	ds_read_b128 v[30:33], v10 offset:20480
	ds_read_b128 v[34:37], v10 offset:22528
	v_readfirstlane_b32 s7, v38
	s_mov_b32 s15, m0
	s_mov_b32 m0, s7
	s_nop 0
	global_load_lds_dwordx4 v[12:13], off
	s_mov_b32 m0, s15
	v_lshl_add_u64 v[12:13], v[6:7], 0, s[24:25]
	v_lshl_add_u64 v[38:39], v[106:107], 0, s[4:5]
	v_or_b32_e32 v105, 0x4000, v62
	v_readfirstlane_b32 s15, v38
	s_mov_b32 s17, m0
	s_mov_b32 m0, s15
	s_nop 0
	global_load_lds_dwordx4 v[12:13], off
	s_mov_b32 m0, s17
	v_add_u32_e32 v12, v11, v104
	v_add_u32_e32 v11, v46, v104
	ds_read_b128 v[38:41], v12
	ds_read_b128 v[42:45], v12 offset:2048
	ds_read_b128 v[46:49], v11 offset:16384
	ds_read_b128 v[50:53], v11 offset:18432
	ds_read_b128 v[54:57], v11 offset:20480
	ds_read_b128 v[58:61], v11 offset:22528
	s_waitcnt lgkmcnt(9)
	v_mfma_f32_16x16x32_f16 v[62:65], v[14:17], v[22:25], 0
	s_waitcnt lgkmcnt(8)
	v_mfma_f32_16x16x32_f16 v[66:69], v[14:17], v[26:29], 0
	s_waitcnt lgkmcnt(7)
	v_mfma_f32_16x16x32_f16 v[70:73], v[14:17], v[30:33], 0
	s_waitcnt lgkmcnt(6)
	v_mfma_f32_16x16x32_f16 v[14:17], v[14:17], v[34:37], 0
	v_mfma_f32_16x16x32_f16 v[22:25], v[18:21], v[22:25], 0
	v_mfma_f32_16x16x32_f16 v[26:29], v[18:21], v[26:29], 0
	v_mfma_f32_16x16x32_f16 v[30:33], v[18:21], v[30:33], 0
	v_mfma_f32_16x16x32_f16 v[18:21], v[18:21], v[34:37], 0
	v_add_u32_e32 v94, 0x18000, v94
	s_mov_b64 s[24:25], 0x180
	s_waitcnt vmcnt(4)
	s_barrier
	v_lshl_add_u64 v[34:35], v[4:5], 0, s[24:25]
	v_readfirstlane_b32 s17, v94
	s_mov_b32 s19, m0
	s_mov_b32 m0, s17
	s_nop 0
	global_load_lds_dwordx4 v[34:35], off
	s_mov_b32 m0, s19
	v_lshl_add_u64 v[36:37], v[94:95], 0, s[0:1]
	v_lshl_add_u64 v[34:35], v[6:7], 0, s[24:25]
	v_readfirstlane_b32 s19, v36
	s_mov_b32 s24, m0
	s_mov_b32 m0, s19
	s_nop 0
	global_load_lds_dwordx4 v[34:35], off
	s_mov_b32 m0, s24
	ds_read_b128 v[34:37], v2 offset:32768
	ds_read_b128 v[74:77], v2 offset:34816
	ds_read_b128 v[78:81], v10 offset:49152
	ds_read_b128 v[82:85], v10 offset:51200
	ds_read_b128 v[86:89], v10 offset:53248
	ds_read_b128 v[90:93], v10 offset:55296
	s_waitcnt lgkmcnt(9)
	v_mfma_f32_16x16x32_f16 v[62:65], v[38:41], v[46:49], v[62:65]
	s_waitcnt lgkmcnt(8)
	v_mfma_f32_16x16x32_f16 v[66:69], v[38:41], v[50:53], v[66:69]
	s_waitcnt lgkmcnt(7)
	v_mfma_f32_16x16x32_f16 v[70:73], v[38:41], v[54:57], v[70:73]
	s_waitcnt lgkmcnt(6)
	v_mfma_f32_16x16x32_f16 v[14:17], v[38:41], v[58:61], v[14:17]
	v_mfma_f32_16x16x32_f16 v[22:25], v[42:45], v[46:49], v[22:25]
	v_mfma_f32_16x16x32_f16 v[26:29], v[42:45], v[50:53], v[26:29]
	v_mfma_f32_16x16x32_f16 v[30:33], v[42:45], v[54:57], v[30:33]
	v_mfma_f32_16x16x32_f16 v[18:21], v[42:45], v[58:61], v[18:21]
	s_mov_b64 s[24:25], 0x22180
	v_lshl_add_u64 v[40:41], v[94:95], 0, s[2:3]
	v_lshl_add_u64 v[38:39], v[4:5], 0, s[24:25]
	v_readfirstlane_b32 s2, v40
	s_mov_b32 s3, m0
	s_mov_b32 m0, s2
	s_nop 0
	global_load_lds_dwordx4 v[38:39], off
	s_mov_b32 m0, s3
	v_lshl_add_u64 v[40:41], v[94:95], 0, s[4:5]
	v_lshl_add_u64 v[38:39], v[6:7], 0, s[24:25]
	v_readfirstlane_b32 s3, v40
	s_mov_b32 s4, m0
	s_mov_b32 m0, s3
	s_nop 0
	global_load_lds_dwordx4 v[38:39], off
	s_mov_b32 m0, s4
	ds_read_b128 v[38:41], v12 offset:32768
	ds_read_b128 v[42:45], v12 offset:34816
	ds_read_b128 v[46:49], v11 offset:49152
	ds_read_b128 v[50:53], v11 offset:51200
	ds_read_b128 v[54:57], v11 offset:53248
	ds_read_b128 v[58:61], v11 offset:55296
	s_waitcnt lgkmcnt(9)
	v_mfma_f32_16x16x32_f16 v[62:65], v[34:37], v[78:81], v[62:65]
	s_waitcnt lgkmcnt(8)
	v_mfma_f32_16x16x32_f16 v[66:69], v[34:37], v[82:85], v[66:69]
	s_waitcnt lgkmcnt(7)
	v_mfma_f32_16x16x32_f16 v[70:73], v[34:37], v[86:89], v[70:73]
	s_waitcnt lgkmcnt(6)
	v_mfma_f32_16x16x32_f16 v[34:37], v[34:37], v[90:93], v[14:17]
	v_mfma_f32_16x16x32_f16 v[22:25], v[74:77], v[78:81], v[22:25]
	v_mfma_f32_16x16x32_f16 v[26:29], v[74:77], v[82:85], v[26:29]
	v_mfma_f32_16x16x32_f16 v[30:33], v[74:77], v[86:89], v[30:33]
	v_mfma_f32_16x16x32_f16 v[16:19], v[74:77], v[90:93], v[18:21]
	s_mov_b64 s[4:5], 0x200
	v_lshl_add_u64 v[14:15], v[4:5], 0, s[4:5]
	s_waitcnt vmcnt(4)
	s_barrier
	s_mov_b32 s24, m0
	s_mov_b32 m0, s22
	s_nop 0
	global_load_lds_dwordx4 v[14:15], off
	s_mov_b32 m0, s24
	v_lshl_add_u64 v[14:15], v[6:7], 0, s[4:5]
	s_mov_b32 s4, m0
	s_mov_b32 m0, s23
	s_nop 0
	global_load_lds_dwordx4 v[14:15], off
	s_mov_b32 m0, s4
	v_add_u32_e32 v15, s26, v102
	v_add_u32_e32 v14, v15, v103
	v_add3_u32 v13, s26, v103, v105
	ds_read_b128 v[74:77], v14
	ds_read_b128 v[78:81], v14 offset:2048
	ds_read_b128 v[82:85], v13
	ds_read_b128 v[86:89], v13 offset:2048
	ds_read_b128 v[90:93], v13 offset:4096
	ds_read_b128 v[94:97], v13 offset:6144
	s_waitcnt lgkmcnt(9)
	v_mfma_f32_16x16x32_f16 v[62:65], v[38:41], v[46:49], v[62:65]
	s_waitcnt lgkmcnt(8)
	v_mfma_f32_16x16x32_f16 v[66:69], v[38:41], v[50:53], v[66:69]
	s_waitcnt lgkmcnt(7)
	v_mfma_f32_16x16x32_f16 v[70:73], v[38:41], v[54:57], v[70:73]
	s_waitcnt lgkmcnt(6)
	v_mfma_f32_16x16x32_f16 v[34:37], v[38:41], v[58:61], v[34:37]
	v_mfma_f32_16x16x32_f16 v[20:23], v[42:45], v[46:49], v[22:25]
	v_mfma_f32_16x16x32_f16 v[24:27], v[42:45], v[50:53], v[26:29]
	v_mfma_f32_16x16x32_f16 v[28:31], v[42:45], v[54:57], v[30:33]
	v_mfma_f32_16x16x32_f16 v[38:41], v[42:45], v[58:61], v[16:19]
	s_mov_b64 s[4:5], 0x22200
	s_nop 1
	v_lshl_add_u64 v[16:17], v[4:5], 0, s[4:5]
	s_mov_b32 s24, m0
	s_mov_b32 m0, s20
	s_nop 0
	global_load_lds_dwordx4 v[16:17], off
	s_mov_b32 m0, s24
	v_lshl_add_u64 v[16:17], v[6:7], 0, s[4:5]
	s_mov_b32 s4, m0
	s_mov_b32 m0, s21
	s_nop 0
	global_load_lds_dwordx4 v[16:17], off
	s_mov_b32 m0, s4
	v_add_u32_e32 v16, v15, v104
	v_add3_u32 v15, s26, v104, v105
	ds_read_b128 v[42:45], v16
	ds_read_b128 v[46:49], v16 offset:2048
	ds_read_b128 v[50:53], v15
	ds_read_b128 v[54:57], v15 offset:2048
	ds_read_b128 v[58:61], v15 offset:4096
	ds_read_b128 v[98:101], v15 offset:6144
	s_waitcnt lgkmcnt(9)
	v_mfma_f32_16x16x32_f16 v[62:65], v[74:77], v[82:85], v[62:65]
	s_waitcnt lgkmcnt(8)
	v_mfma_f32_16x16x32_f16 v[66:69], v[74:77], v[86:89], v[66:69]
	s_waitcnt lgkmcnt(7)
	v_mfma_f32_16x16x32_f16 v[70:73], v[74:77], v[90:93], v[70:73]
	s_waitcnt lgkmcnt(6)
	v_mfma_f32_16x16x32_f16 v[32:35], v[74:77], v[94:97], v[34:37]
	v_mfma_f32_16x16x32_f16 v[20:23], v[78:81], v[82:85], v[20:23]
	v_mfma_f32_16x16x32_f16 v[24:27], v[78:81], v[86:89], v[24:27]
	v_mfma_f32_16x16x32_f16 v[28:31], v[78:81], v[90:93], v[28:31]
	v_mfma_f32_16x16x32_f16 v[36:39], v[78:81], v[94:97], v[38:41]
	s_mov_b64 s[4:5], 0x280
	s_waitcnt vmcnt(4)
	s_barrier
	v_lshl_add_u64 v[18:19], v[4:5], 0, s[4:5]
	s_mov_b32 s24, m0
	s_mov_b32 m0, s16
	s_nop 0
	global_load_lds_dwordx4 v[18:19], off
	s_mov_b32 m0, s24
	v_lshl_add_u64 v[18:19], v[6:7], 0, s[4:5]
	s_add_i32 s24, 0, 0x18000
	s_mov_b32 s4, m0
	s_mov_b32 m0, s18
	s_nop 0
	global_load_lds_dwordx4 v[18:19], off
	s_mov_b32 m0, s4
	v_add_u32_e32 v19, s24, v102
	v_add_u32_e32 v17, v19, v103
	v_add3_u32 v18, s24, v103, v105
	ds_read_b128 v[74:77], v17
	ds_read_b128 v[78:81], v17 offset:2048
	ds_read_b128 v[82:85], v18
	ds_read_b128 v[86:89], v18 offset:2048
	ds_read_b128 v[90:93], v18 offset:4096
	ds_read_b128 v[94:97], v18 offset:6144
	s_waitcnt lgkmcnt(9)
	v_mfma_f32_16x16x32_f16 v[62:65], v[42:45], v[50:53], v[62:65]
	s_waitcnt lgkmcnt(8)
	v_mfma_f32_16x16x32_f16 v[66:69], v[42:45], v[54:57], v[66:69]
	s_waitcnt lgkmcnt(7)
	v_mfma_f32_16x16x32_f16 v[70:73], v[42:45], v[58:61], v[70:73]
	s_waitcnt lgkmcnt(6)
	v_mfma_f32_16x16x32_f16 v[32:35], v[42:45], v[98:101], v[32:35]
	v_mfma_f32_16x16x32_f16 v[40:43], v[46:49], v[50:53], v[20:23]
	v_mfma_f32_16x16x32_f16 v[22:25], v[46:49], v[54:57], v[24:27]
	v_mfma_f32_16x16x32_f16 v[26:29], v[46:49], v[58:61], v[28:31]
	v_mfma_f32_16x16x32_f16 v[36:39], v[46:49], v[98:101], v[36:39]
	s_mov_b64 s[4:5], 0x22280
	v_lshl_add_u64 v[20:21], v[4:5], 0, s[4:5]
	s_mov_b32 s25, m0
	s_mov_b32 m0, s6
	s_nop 0
	global_load_lds_dwordx4 v[20:21], off
	s_mov_b32 m0, s25
	v_lshl_add_u64 v[20:21], v[6:7], 0, s[4:5]
	s_mov_b32 s4, m0
	s_mov_b32 m0, s14
	s_nop 0
	global_load_lds_dwordx4 v[20:21], off
	s_mov_b32 m0, s4
	v_add_u32_e32 v19, v19, v104
	v_add3_u32 v20, s24, v104, v105
	ds_read_b128 v[44:47], v19
	ds_read_b128 v[48:51], v19 offset:2048
	ds_read_b128 v[52:55], v20
	ds_read_b128 v[56:59], v20 offset:2048
	ds_read_b128 v[98:101], v20 offset:4096
	ds_read_b128 v[102:105], v20 offset:6144
	s_waitcnt lgkmcnt(9)
	v_mfma_f32_16x16x32_f16 v[60:63], v[74:77], v[82:85], v[62:65]
	s_waitcnt lgkmcnt(8)
	v_mfma_f32_16x16x32_f16 v[64:67], v[74:77], v[86:89], v[66:69]
	s_waitcnt lgkmcnt(7)
	v_mfma_f32_16x16x32_f16 v[68:71], v[74:77], v[90:93], v[70:73]
	s_waitcnt lgkmcnt(6)
	v_mfma_f32_16x16x32_f16 v[30:33], v[74:77], v[94:97], v[32:35]
	v_mfma_f32_16x16x32_f16 v[40:43], v[78:81], v[82:85], v[40:43]
	v_mfma_f32_16x16x32_f16 v[22:25], v[78:81], v[86:89], v[22:25]
	v_mfma_f32_16x16x32_f16 v[26:29], v[78:81], v[90:93], v[26:29]
	v_mfma_f32_16x16x32_f16 v[34:37], v[78:81], v[94:97], v[36:39]
	s_mov_b64 s[24:25], 0x300
	s_waitcnt vmcnt(4)
	s_barrier
	s_nop 0
	v_lshl_add_u64 v[38:39], v[4:5], 0, s[24:25]
	v_readfirstlane_b32 s4, v106
	s_mov_b32 s5, m0
	s_mov_b32 m0, s4
	s_nop 0
	global_load_lds_dwordx4 v[38:39], off
	s_mov_b32 m0, s5
	v_lshl_add_u64 v[72:73], v[106:107], 0, s[0:1]
	v_lshl_add_u64 v[38:39], v[6:7], 0, s[24:25]
	v_readfirstlane_b32 s0, v72
	s_mov_b32 s1, m0
	s_mov_b32 m0, s0
	s_nop 0
	global_load_lds_dwordx4 v[38:39], off
	s_mov_b32 m0, s1
	ds_read_b128 v[72:75], v2
	ds_read_b128 v[76:79], v2 offset:2048
	ds_read_b128 v[80:83], v10 offset:16384
	ds_read_b128 v[84:87], v10 offset:18432
	ds_read_b128 v[88:91], v10 offset:20480
	ds_read_b128 v[92:95], v10 offset:22528
	s_waitcnt lgkmcnt(9)
	v_mfma_f32_16x16x32_f16 v[60:63], v[44:47], v[52:55], v[60:63]
	s_waitcnt lgkmcnt(8)
	v_mfma_f32_16x16x32_f16 v[64:67], v[44:47], v[56:59], v[64:67]
	s_waitcnt lgkmcnt(7)
	v_mfma_f32_16x16x32_f16 v[68:71], v[44:47], v[98:101], v[68:71]
	s_waitcnt lgkmcnt(6)
	v_mfma_f32_16x16x32_f16 v[30:33], v[44:47], v[102:105], v[30:33]
	v_mfma_f32_16x16x32_f16 v[38:41], v[48:51], v[52:55], v[40:43]
	v_mfma_f32_16x16x32_f16 v[22:25], v[48:51], v[56:59], v[22:25]
	v_mfma_f32_16x16x32_f16 v[26:29], v[48:51], v[98:101], v[26:29]
	v_mfma_f32_16x16x32_f16 v[34:37], v[48:51], v[102:105], v[34:37]
	s_mov_b64 s[24:25], 0x22300
	v_lshl_add_u64 v[42:43], v[4:5], 0, s[24:25]
	s_mov_b32 s1, m0
	s_mov_b32 m0, s7
	s_nop 0
	global_load_lds_dwordx4 v[42:43], off
	s_mov_b32 m0, s1
	v_lshl_add_u64 v[42:43], v[6:7], 0, s[24:25]
	s_mov_b32 s1, m0
	s_mov_b32 m0, s15
	s_nop 0
	global_load_lds_dwordx4 v[42:43], off
	s_mov_b32 m0, s1
	ds_read_b128 v[42:45], v12
	ds_read_b128 v[46:49], v12 offset:2048
	ds_read_b128 v[50:53], v11 offset:16384
	ds_read_b128 v[54:57], v11 offset:18432
	ds_read_b128 v[96:99], v11 offset:20480
	ds_read_b128 v[100:103], v11 offset:22528
	s_waitcnt lgkmcnt(9)
	v_mfma_f32_16x16x32_f16 v[58:61], v[72:75], v[80:83], v[60:63]
	s_waitcnt lgkmcnt(8)
	v_mfma_f32_16x16x32_f16 v[62:65], v[72:75], v[84:87], v[64:67]
	s_waitcnt lgkmcnt(7)
	v_mfma_f32_16x16x32_f16 v[66:69], v[72:75], v[88:91], v[68:71]
	s_waitcnt lgkmcnt(6)
	v_mfma_f32_16x16x32_f16 v[30:33], v[72:75], v[92:95], v[30:33]
	v_mfma_f32_16x16x32_f16 v[38:41], v[76:79], v[80:83], v[38:41]
	v_mfma_f32_16x16x32_f16 v[22:25], v[76:79], v[84:87], v[22:25]
	v_mfma_f32_16x16x32_f16 v[26:29], v[76:79], v[88:91], v[26:29]
	v_mfma_f32_16x16x32_f16 v[34:37], v[76:79], v[92:95], v[34:37]
	s_mov_b64 s[24:25], 0x380
	s_waitcnt vmcnt(4)
	s_barrier
	v_lshl_add_u64 v[70:71], v[4:5], 0, s[24:25]
	s_mov_b32 s1, m0
	s_mov_b32 m0, s17
	s_nop 0
	global_load_lds_dwordx4 v[70:71], off
	s_mov_b32 m0, s1
	v_lshl_add_u64 v[70:71], v[6:7], 0, s[24:25]
	s_mov_b32 s1, m0
	s_mov_b32 m0, s19
	s_nop 0
	global_load_lds_dwordx4 v[70:71], off
	s_mov_b32 m0, s1
	ds_read_b128 v[70:73], v2 offset:32768
	ds_read_b128 v[74:77], v2 offset:34816
	ds_read_b128 v[78:81], v10 offset:49152
	ds_read_b128 v[82:85], v10 offset:51200
	ds_read_b128 v[86:89], v10 offset:53248
	ds_read_b128 v[90:93], v10 offset:55296
	s_waitcnt lgkmcnt(9)
	v_mfma_f32_16x16x32_f16 v[58:61], v[42:45], v[50:53], v[58:61]
	s_waitcnt lgkmcnt(8)
	v_mfma_f32_16x16x32_f16 v[62:65], v[42:45], v[54:57], v[62:65]
	s_waitcnt lgkmcnt(7)
	v_mfma_f32_16x16x32_f16 v[66:69], v[42:45], v[96:99], v[66:69]
	s_waitcnt lgkmcnt(6)
	v_mfma_f32_16x16x32_f16 v[30:33], v[42:45], v[100:103], v[30:33]
	v_mfma_f32_16x16x32_f16 v[38:41], v[46:49], v[50:53], v[38:41]
	v_mfma_f32_16x16x32_f16 v[22:25], v[46:49], v[54:57], v[22:25]
	v_mfma_f32_16x16x32_f16 v[26:29], v[46:49], v[96:99], v[26:29]
	v_mfma_f32_16x16x32_f16 v[34:37], v[46:49], v[100:103], v[34:37]
	s_mov_b64 s[24:25], 0x22380
	v_lshl_add_u64 v[42:43], v[4:5], 0, s[24:25]
	s_mov_b32 s1, m0
	s_mov_b32 m0, s2
	s_nop 0
	global_load_lds_dwordx4 v[42:43], off
	s_mov_b32 m0, s1
	v_lshl_add_u64 v[42:43], v[6:7], 0, s[24:25]
	s_mov_b32 s1, m0
	s_mov_b32 m0, s3
	s_nop 0
	global_load_lds_dwordx4 v[42:43], off
	s_mov_b32 m0, s1
	ds_read_b128 v[42:45], v12 offset:32768
	ds_read_b128 v[46:49], v12 offset:34816
	ds_read_b128 v[50:53], v11 offset:49152
	ds_read_b128 v[54:57], v11 offset:51200
	ds_read_b128 v[94:97], v11 offset:53248
	ds_read_b128 v[98:101], v11 offset:55296
	s_waitcnt lgkmcnt(9)
	v_mfma_f32_16x16x32_f16 v[58:61], v[70:73], v[78:81], v[58:61]
	s_waitcnt lgkmcnt(8)
	v_mfma_f32_16x16x32_f16 v[62:65], v[70:73], v[82:85], v[62:65]
	s_waitcnt lgkmcnt(7)
	v_mfma_f32_16x16x32_f16 v[66:69], v[70:73], v[86:89], v[66:69]
	s_waitcnt lgkmcnt(6)
	v_mfma_f32_16x16x32_f16 v[30:33], v[70:73], v[90:93], v[30:33]
	v_mfma_f32_16x16x32_f16 v[38:41], v[74:77], v[78:81], v[38:41]
	v_mfma_f32_16x16x32_f16 v[22:25], v[74:77], v[82:85], v[22:25]
	v_mfma_f32_16x16x32_f16 v[26:29], v[74:77], v[86:89], v[26:29]
	v_mfma_f32_16x16x32_f16 v[34:37], v[74:77], v[90:93], v[34:37]
	s_mov_b64 s[24:25], 0x400
	s_waitcnt vmcnt(4)
	s_barrier
	v_lshl_add_u64 v[70:71], v[4:5], 0, s[24:25]
	s_mov_b32 s1, m0
	s_mov_b32 m0, s22
	s_nop 0
	global_load_lds_dwordx4 v[70:71], off
	s_mov_b32 m0, s1
	v_lshl_add_u64 v[70:71], v[6:7], 0, s[24:25]
	s_mov_b32 s1, m0
	s_mov_b32 m0, s23
	s_nop 0
	global_load_lds_dwordx4 v[70:71], off
	s_mov_b32 m0, s1
	ds_read_b128 v[70:73], v14
	ds_read_b128 v[74:77], v14 offset:2048
	ds_read_b128 v[78:81], v13
	ds_read_b128 v[82:85], v13 offset:2048
	ds_read_b128 v[86:89], v13 offset:4096
	ds_read_b128 v[90:93], v13 offset:6144
	s_waitcnt lgkmcnt(9)
	v_mfma_f32_16x16x32_f16 v[58:61], v[42:45], v[50:53], v[58:61]
	s_waitcnt lgkmcnt(8)
	v_mfma_f32_16x16x32_f16 v[62:65], v[42:45], v[54:57], v[62:65]
	s_waitcnt lgkmcnt(7)
	v_mfma_f32_16x16x32_f16 v[66:69], v[42:45], v[94:97], v[66:69]
	s_waitcnt lgkmcnt(6)
	v_mfma_f32_16x16x32_f16 v[30:33], v[42:45], v[98:101], v[30:33]
	v_mfma_f32_16x16x32_f16 v[38:41], v[46:49], v[50:53], v[38:41]
	v_mfma_f32_16x16x32_f16 v[22:25], v[46:49], v[54:57], v[22:25]
	v_mfma_f32_16x16x32_f16 v[26:29], v[46:49], v[94:97], v[26:29]
	v_mfma_f32_16x16x32_f16 v[34:37], v[46:49], v[98:101], v[34:37]
	s_mov_b64 s[24:25], 0x22400
	v_lshl_add_u64 v[42:43], v[4:5], 0, s[24:25]
	s_mov_b32 s1, m0
	s_mov_b32 m0, s20
	s_nop 0
	global_load_lds_dwordx4 v[42:43], off
	s_mov_b32 m0, s1
	v_lshl_add_u64 v[42:43], v[6:7], 0, s[24:25]
	s_mov_b32 s1, m0
	s_mov_b32 m0, s21
	s_nop 0
	global_load_lds_dwordx4 v[42:43], off
	s_mov_b32 m0, s1
	ds_read_b128 v[42:45], v16
	ds_read_b128 v[46:49], v16 offset:2048
	ds_read_b128 v[50:53], v15
	ds_read_b128 v[54:57], v15 offset:2048
	ds_read_b128 v[94:97], v15 offset:4096
	ds_read_b128 v[98:101], v15 offset:6144
	s_waitcnt lgkmcnt(9)
	v_mfma_f32_16x16x32_f16 v[58:61], v[70:73], v[78:81], v[58:61]
	s_waitcnt lgkmcnt(8)
	v_mfma_f32_16x16x32_f16 v[62:65], v[70:73], v[82:85], v[62:65]
	s_waitcnt lgkmcnt(7)
	v_mfma_f32_16x16x32_f16 v[66:69], v[70:73], v[86:89], v[66:69]
	s_waitcnt lgkmcnt(6)
	v_mfma_f32_16x16x32_f16 v[30:33], v[70:73], v[90:93], v[30:33]
	v_mfma_f32_16x16x32_f16 v[38:41], v[74:77], v[78:81], v[38:41]
	v_mfma_f32_16x16x32_f16 v[22:25], v[74:77], v[82:85], v[22:25]
	v_mfma_f32_16x16x32_f16 v[26:29], v[74:77], v[86:89], v[26:29]
	v_mfma_f32_16x16x32_f16 v[34:37], v[74:77], v[90:93], v[34:37]
	s_mov_b64 s[24:25], 0x480
	s_waitcnt vmcnt(4)
	s_barrier
	v_lshl_add_u64 v[70:71], v[4:5], 0, s[24:25]
	s_mov_b32 s1, m0
	s_mov_b32 m0, s16
	s_nop 0
	global_load_lds_dwordx4 v[70:71], off
	s_mov_b32 m0, s1
	v_lshl_add_u64 v[70:71], v[6:7], 0, s[24:25]
	s_mov_b32 s1, m0
	s_mov_b32 m0, s18
	s_nop 0
	global_load_lds_dwordx4 v[70:71], off
	s_mov_b32 m0, s1
	ds_read_b128 v[70:73], v17
	ds_read_b128 v[74:77], v17 offset:2048
	ds_read_b128 v[78:81], v18
	ds_read_b128 v[82:85], v18 offset:2048
	ds_read_b128 v[86:89], v18 offset:4096
	ds_read_b128 v[90:93], v18 offset:6144
	s_waitcnt lgkmcnt(9)
	v_mfma_f32_16x16x32_f16 v[58:61], v[42:45], v[50:53], v[58:61]
	s_waitcnt lgkmcnt(8)
	v_mfma_f32_16x16x32_f16 v[62:65], v[42:45], v[54:57], v[62:65]
	s_waitcnt lgkmcnt(7)
	v_mfma_f32_16x16x32_f16 v[66:69], v[42:45], v[94:97], v[66:69]
	s_waitcnt lgkmcnt(6)
	v_mfma_f32_16x16x32_f16 v[30:33], v[42:45], v[98:101], v[30:33]
	v_mfma_f32_16x16x32_f16 v[38:41], v[46:49], v[50:53], v[38:41]
	v_mfma_f32_16x16x32_f16 v[22:25], v[46:49], v[54:57], v[22:25]
	v_mfma_f32_16x16x32_f16 v[26:29], v[46:49], v[94:97], v[26:29]
	v_mfma_f32_16x16x32_f16 v[34:37], v[46:49], v[98:101], v[34:37]
	s_mov_b64 s[24:25], 0x22480
	v_lshl_add_u64 v[42:43], v[4:5], 0, s[24:25]
	s_mov_b32 s1, m0
	s_mov_b32 m0, s6
	s_nop 0
	global_load_lds_dwordx4 v[42:43], off
	s_mov_b32 m0, s1
	v_lshl_add_u64 v[42:43], v[6:7], 0, s[24:25]
	s_mov_b32 s1, m0
	s_mov_b32 m0, s14
	s_nop 0
	global_load_lds_dwordx4 v[42:43], off
	s_mov_b32 m0, s1
	ds_read_b128 v[42:45], v19
	ds_read_b128 v[46:49], v19 offset:2048
	ds_read_b128 v[50:53], v20
	ds_read_b128 v[54:57], v20 offset:2048
	ds_read_b128 v[94:97], v20 offset:4096
	ds_read_b128 v[98:101], v20 offset:6144
	s_waitcnt lgkmcnt(9)
	v_mfma_f32_16x16x32_f16 v[58:61], v[70:73], v[78:81], v[58:61]
	s_waitcnt lgkmcnt(8)
	v_mfma_f32_16x16x32_f16 v[62:65], v[70:73], v[82:85], v[62:65]
	s_waitcnt lgkmcnt(7)
	v_mfma_f32_16x16x32_f16 v[66:69], v[70:73], v[86:89], v[66:69]
	s_waitcnt lgkmcnt(6)
	v_mfma_f32_16x16x32_f16 v[30:33], v[70:73], v[90:93], v[30:33]
	v_mfma_f32_16x16x32_f16 v[38:41], v[74:77], v[78:81], v[38:41]
	v_mfma_f32_16x16x32_f16 v[22:25], v[74:77], v[82:85], v[22:25]
	v_mfma_f32_16x16x32_f16 v[26:29], v[74:77], v[86:89], v[26:29]
	v_mfma_f32_16x16x32_f16 v[34:37], v[74:77], v[90:93], v[34:37]
	s_mov_b64 s[24:25], 0x500
	s_waitcnt vmcnt(4)
	s_barrier
	v_lshl_add_u64 v[70:71], v[4:5], 0, s[24:25]
	s_mov_b32 s1, m0
	s_mov_b32 m0, s4
	s_nop 0
	global_load_lds_dwordx4 v[70:71], off
	s_mov_b32 m0, s1
	v_lshl_add_u64 v[70:71], v[6:7], 0, s[24:25]
	s_mov_b32 s1, m0
	s_mov_b32 m0, s0
	s_nop 0
	global_load_lds_dwordx4 v[70:71], off
	s_mov_b32 m0, s1
	ds_read_b128 v[70:73], v2
	ds_read_b128 v[74:77], v2 offset:2048
	ds_read_b128 v[78:81], v10 offset:16384
	ds_read_b128 v[82:85], v10 offset:18432
	ds_read_b128 v[86:89], v10 offset:20480
	ds_read_b128 v[90:93], v10 offset:22528
	s_waitcnt lgkmcnt(9)
	v_mfma_f32_16x16x32_f16 v[58:61], v[42:45], v[50:53], v[58:61]
	s_waitcnt lgkmcnt(8)
	v_mfma_f32_16x16x32_f16 v[62:65], v[42:45], v[54:57], v[62:65]
	s_waitcnt lgkmcnt(7)
	v_mfma_f32_16x16x32_f16 v[66:69], v[42:45], v[94:97], v[66:69]
	s_waitcnt lgkmcnt(6)
	v_mfma_f32_16x16x32_f16 v[30:33], v[42:45], v[98:101], v[30:33]
	v_mfma_f32_16x16x32_f16 v[38:41], v[46:49], v[50:53], v[38:41]
	v_mfma_f32_16x16x32_f16 v[22:25], v[46:49], v[54:57], v[22:25]
	v_mfma_f32_16x16x32_f16 v[26:29], v[46:49], v[94:97], v[26:29]
	v_mfma_f32_16x16x32_f16 v[34:37], v[46:49], v[98:101], v[34:37]
	s_mov_b64 s[24:25], 0x22500
	v_lshl_add_u64 v[42:43], v[4:5], 0, s[24:25]
	s_mov_b32 s1, m0
	s_mov_b32 m0, s7
	s_nop 0
	global_load_lds_dwordx4 v[42:43], off
	s_mov_b32 m0, s1
	v_lshl_add_u64 v[42:43], v[6:7], 0, s[24:25]
	s_mov_b32 s1, m0
	s_mov_b32 m0, s15
	s_nop 0
	global_load_lds_dwordx4 v[42:43], off
	s_mov_b32 m0, s1
	ds_read_b128 v[42:45], v12
	ds_read_b128 v[46:49], v12 offset:2048
	ds_read_b128 v[50:53], v11 offset:16384
	ds_read_b128 v[54:57], v11 offset:18432
	ds_read_b128 v[94:97], v11 offset:20480
	ds_read_b128 v[98:101], v11 offset:22528
	s_waitcnt lgkmcnt(9)
	v_mfma_f32_16x16x32_f16 v[58:61], v[70:73], v[78:81], v[58:61]
	s_waitcnt lgkmcnt(8)
	v_mfma_f32_16x16x32_f16 v[62:65], v[70:73], v[82:85], v[62:65]
	s_waitcnt lgkmcnt(7)
	v_mfma_f32_16x16x32_f16 v[66:69], v[70:73], v[86:89], v[66:69]
	s_waitcnt lgkmcnt(6)
	v_mfma_f32_16x16x32_f16 v[30:33], v[70:73], v[90:93], v[30:33]
	v_mfma_f32_16x16x32_f16 v[38:41], v[74:77], v[78:81], v[38:41]
	v_mfma_f32_16x16x32_f16 v[22:25], v[74:77], v[82:85], v[22:25]
	v_mfma_f32_16x16x32_f16 v[26:29], v[74:77], v[86:89], v[26:29]
	v_mfma_f32_16x16x32_f16 v[34:37], v[74:77], v[90:93], v[34:37]
	s_mov_b64 s[24:25], 0x580
	s_waitcnt vmcnt(4)
	s_barrier
	v_lshl_add_u64 v[70:71], v[4:5], 0, s[24:25]
	s_mov_b32 s1, m0
	s_mov_b32 m0, s17
	s_nop 0
	global_load_lds_dwordx4 v[70:71], off
	s_mov_b32 m0, s1
	v_lshl_add_u64 v[70:71], v[6:7], 0, s[24:25]
	s_mov_b32 s1, m0
	s_mov_b32 m0, s19
	s_nop 0
	global_load_lds_dwordx4 v[70:71], off
	s_mov_b32 m0, s1
	ds_read_b128 v[70:73], v2 offset:32768
	ds_read_b128 v[74:77], v2 offset:34816
	ds_read_b128 v[78:81], v10 offset:49152
	ds_read_b128 v[82:85], v10 offset:51200
	ds_read_b128 v[86:89], v10 offset:53248
	ds_read_b128 v[90:93], v10 offset:55296
	s_waitcnt lgkmcnt(9)
	v_mfma_f32_16x16x32_f16 v[58:61], v[42:45], v[50:53], v[58:61]
	s_waitcnt lgkmcnt(8)
	v_mfma_f32_16x16x32_f16 v[62:65], v[42:45], v[54:57], v[62:65]
	s_waitcnt lgkmcnt(7)
	v_mfma_f32_16x16x32_f16 v[66:69], v[42:45], v[94:97], v[66:69]
	s_waitcnt lgkmcnt(6)
	v_mfma_f32_16x16x32_f16 v[30:33], v[42:45], v[98:101], v[30:33]
	v_mfma_f32_16x16x32_f16 v[38:41], v[46:49], v[50:53], v[38:41]
	v_mfma_f32_16x16x32_f16 v[22:25], v[46:49], v[54:57], v[22:25]
	v_mfma_f32_16x16x32_f16 v[26:29], v[46:49], v[94:97], v[26:29]
	v_mfma_f32_16x16x32_f16 v[34:37], v[46:49], v[98:101], v[34:37]
	s_mov_b64 s[24:25], 0x22580
	v_lshl_add_u64 v[42:43], v[4:5], 0, s[24:25]
	s_mov_b32 s1, m0
	s_mov_b32 m0, s2
	s_nop 0
	global_load_lds_dwordx4 v[42:43], off
	s_mov_b32 m0, s1
	v_lshl_add_u64 v[42:43], v[6:7], 0, s[24:25]
	s_mov_b32 s1, m0
	s_mov_b32 m0, s3
	s_nop 0
	global_load_lds_dwordx4 v[42:43], off
	s_mov_b32 m0, s1
	ds_read_b128 v[42:45], v12 offset:32768
	ds_read_b128 v[46:49], v12 offset:34816
	ds_read_b128 v[50:53], v11 offset:49152
	ds_read_b128 v[54:57], v11 offset:51200
	ds_read_b128 v[94:97], v11 offset:53248
	ds_read_b128 v[98:101], v11 offset:55296
	s_waitcnt lgkmcnt(9)
	v_mfma_f32_16x16x32_f16 v[58:61], v[70:73], v[78:81], v[58:61]
	s_waitcnt lgkmcnt(8)
	v_mfma_f32_16x16x32_f16 v[62:65], v[70:73], v[82:85], v[62:65]
	s_waitcnt lgkmcnt(7)
	v_mfma_f32_16x16x32_f16 v[66:69], v[70:73], v[86:89], v[66:69]
	s_waitcnt lgkmcnt(6)
	v_mfma_f32_16x16x32_f16 v[30:33], v[70:73], v[90:93], v[30:33]
	v_mfma_f32_16x16x32_f16 v[38:41], v[74:77], v[78:81], v[38:41]
	v_mfma_f32_16x16x32_f16 v[22:25], v[74:77], v[82:85], v[22:25]
	v_mfma_f32_16x16x32_f16 v[26:29], v[74:77], v[86:89], v[26:29]
	v_mfma_f32_16x16x32_f16 v[34:37], v[74:77], v[90:93], v[34:37]
	s_mov_b64 s[24:25], 0x600
	s_waitcnt vmcnt(4)
	s_barrier
	v_lshl_add_u64 v[70:71], v[4:5], 0, s[24:25]
	s_mov_b32 s1, m0
	s_mov_b32 m0, s22
	s_nop 0
	global_load_lds_dwordx4 v[70:71], off
	s_mov_b32 m0, s1
	v_lshl_add_u64 v[70:71], v[6:7], 0, s[24:25]
	s_mov_b32 s1, m0
	s_mov_b32 m0, s23
	s_nop 0
	global_load_lds_dwordx4 v[70:71], off
	s_mov_b32 m0, s1
	ds_read_b128 v[70:73], v14
	ds_read_b128 v[74:77], v14 offset:2048
	ds_read_b128 v[78:81], v13
	ds_read_b128 v[82:85], v13 offset:2048
	ds_read_b128 v[86:89], v13 offset:4096
	ds_read_b128 v[90:93], v13 offset:6144
	s_waitcnt lgkmcnt(9)
	v_mfma_f32_16x16x32_f16 v[58:61], v[42:45], v[50:53], v[58:61]
	s_waitcnt lgkmcnt(8)
	v_mfma_f32_16x16x32_f16 v[62:65], v[42:45], v[54:57], v[62:65]
	s_waitcnt lgkmcnt(7)
	v_mfma_f32_16x16x32_f16 v[66:69], v[42:45], v[94:97], v[66:69]
	s_waitcnt lgkmcnt(6)
	v_mfma_f32_16x16x32_f16 v[30:33], v[42:45], v[98:101], v[30:33]
	v_mfma_f32_16x16x32_f16 v[38:41], v[46:49], v[50:53], v[38:41]
	v_mfma_f32_16x16x32_f16 v[22:25], v[46:49], v[54:57], v[22:25]
	v_mfma_f32_16x16x32_f16 v[26:29], v[46:49], v[94:97], v[26:29]
	v_mfma_f32_16x16x32_f16 v[34:37], v[46:49], v[98:101], v[34:37]
	s_mov_b64 s[22:23], 0x22600
	v_lshl_add_u64 v[42:43], v[4:5], 0, s[22:23]
	s_mov_b32 s1, m0
	s_mov_b32 m0, s20
	s_nop 0
	global_load_lds_dwordx4 v[42:43], off
	s_mov_b32 m0, s1
	v_lshl_add_u64 v[42:43], v[6:7], 0, s[22:23]
	s_mov_b32 s1, m0
	s_mov_b32 m0, s21
	s_nop 0
	global_load_lds_dwordx4 v[42:43], off
	s_mov_b32 m0, s1
	ds_read_b128 v[42:45], v16
	ds_read_b128 v[46:49], v16 offset:2048
	ds_read_b128 v[50:53], v15
	ds_read_b128 v[54:57], v15 offset:2048
	ds_read_b128 v[94:97], v15 offset:4096
	ds_read_b128 v[98:101], v15 offset:6144
	s_waitcnt lgkmcnt(9)
	v_mfma_f32_16x16x32_f16 v[58:61], v[70:73], v[78:81], v[58:61]
	s_waitcnt lgkmcnt(8)
	v_mfma_f32_16x16x32_f16 v[62:65], v[70:73], v[82:85], v[62:65]
	s_waitcnt lgkmcnt(7)
	v_mfma_f32_16x16x32_f16 v[66:69], v[70:73], v[86:89], v[66:69]
	s_waitcnt lgkmcnt(6)
	v_mfma_f32_16x16x32_f16 v[30:33], v[70:73], v[90:93], v[30:33]
	v_mfma_f32_16x16x32_f16 v[38:41], v[74:77], v[78:81], v[38:41]
	v_mfma_f32_16x16x32_f16 v[22:25], v[74:77], v[82:85], v[22:25]
	v_mfma_f32_16x16x32_f16 v[26:29], v[74:77], v[86:89], v[26:29]
	v_mfma_f32_16x16x32_f16 v[34:37], v[74:77], v[90:93], v[34:37]
	s_mov_b64 s[20:21], 0x680
	s_waitcnt vmcnt(4)
	s_barrier
	v_lshl_add_u64 v[70:71], v[4:5], 0, s[20:21]
	s_mov_b32 s1, m0
	s_mov_b32 m0, s16
	s_nop 0
	global_load_lds_dwordx4 v[70:71], off
	s_mov_b32 m0, s1
	v_lshl_add_u64 v[70:71], v[6:7], 0, s[20:21]
	s_mov_b32 s1, m0
	s_mov_b32 m0, s18
	s_nop 0
	global_load_lds_dwordx4 v[70:71], off
	s_mov_b32 m0, s1
	ds_read_b128 v[70:73], v17
	ds_read_b128 v[74:77], v17 offset:2048
	ds_read_b128 v[78:81], v18
	ds_read_b128 v[82:85], v18 offset:2048
	ds_read_b128 v[86:89], v18 offset:4096
	ds_read_b128 v[90:93], v18 offset:6144
	s_waitcnt lgkmcnt(9)
	v_mfma_f32_16x16x32_f16 v[58:61], v[42:45], v[50:53], v[58:61]
	s_waitcnt lgkmcnt(8)
	v_mfma_f32_16x16x32_f16 v[62:65], v[42:45], v[54:57], v[62:65]
	s_waitcnt lgkmcnt(7)
	v_mfma_f32_16x16x32_f16 v[66:69], v[42:45], v[94:97], v[66:69]
	s_waitcnt lgkmcnt(6)
	v_mfma_f32_16x16x32_f16 v[30:33], v[42:45], v[98:101], v[30:33]
	v_mfma_f32_16x16x32_f16 v[38:41], v[46:49], v[50:53], v[38:41]
	v_mfma_f32_16x16x32_f16 v[22:25], v[46:49], v[54:57], v[22:25]
	v_mfma_f32_16x16x32_f16 v[26:29], v[46:49], v[94:97], v[26:29]
	v_mfma_f32_16x16x32_f16 v[34:37], v[46:49], v[98:101], v[34:37]
	s_mov_b64 s[20:21], 0x22680
	v_lshl_add_u64 v[42:43], v[4:5], 0, s[20:21]
	s_mov_b32 s1, m0
	s_mov_b32 m0, s6
	s_nop 0
	global_load_lds_dwordx4 v[42:43], off
	s_mov_b32 m0, s1
	v_lshl_add_u64 v[42:43], v[6:7], 0, s[20:21]
	s_mov_b32 s1, m0
	s_mov_b32 m0, s14
	s_nop 0
	global_load_lds_dwordx4 v[42:43], off
	s_mov_b32 m0, s1
	ds_read_b128 v[42:45], v19
	ds_read_b128 v[46:49], v19 offset:2048
	ds_read_b128 v[50:53], v20
	ds_read_b128 v[54:57], v20 offset:2048
	ds_read_b128 v[94:97], v20 offset:4096
	ds_read_b128 v[98:101], v20 offset:6144
	s_waitcnt lgkmcnt(9)
	v_mfma_f32_16x16x32_f16 v[58:61], v[70:73], v[78:81], v[58:61]
	s_waitcnt lgkmcnt(8)
	v_mfma_f32_16x16x32_f16 v[62:65], v[70:73], v[82:85], v[62:65]
	s_waitcnt lgkmcnt(7)
	v_mfma_f32_16x16x32_f16 v[66:69], v[70:73], v[86:89], v[66:69]
	s_waitcnt lgkmcnt(6)
	v_mfma_f32_16x16x32_f16 v[30:33], v[70:73], v[90:93], v[30:33]
	v_mfma_f32_16x16x32_f16 v[38:41], v[74:77], v[78:81], v[38:41]
	v_mfma_f32_16x16x32_f16 v[22:25], v[74:77], v[82:85], v[22:25]
	v_mfma_f32_16x16x32_f16 v[26:29], v[74:77], v[86:89], v[26:29]
	v_mfma_f32_16x16x32_f16 v[34:37], v[74:77], v[90:93], v[34:37]
	s_mov_b64 s[20:21], 0x700
	s_waitcnt vmcnt(4)
	s_barrier
	v_lshl_add_u64 v[70:71], v[4:5], 0, s[20:21]
	s_mov_b32 s1, m0
	s_mov_b32 m0, s4
	s_nop 0
	global_load_lds_dwordx4 v[70:71], off
	s_mov_b32 m0, s1
	v_lshl_add_u64 v[70:71], v[6:7], 0, s[20:21]
	s_mov_b32 s1, m0
	s_mov_b32 m0, s0
	s_nop 0
	global_load_lds_dwordx4 v[70:71], off
	s_mov_b32 m0, s1
	ds_read_b128 v[70:73], v2
	ds_read_b128 v[74:77], v2 offset:2048
	ds_read_b128 v[78:81], v10 offset:16384
	ds_read_b128 v[82:85], v10 offset:18432
	ds_read_b128 v[86:89], v10 offset:20480
	ds_read_b128 v[90:93], v10 offset:22528
	s_waitcnt lgkmcnt(9)
	v_mfma_f32_16x16x32_f16 v[58:61], v[42:45], v[50:53], v[58:61]
	s_waitcnt lgkmcnt(8)
	v_mfma_f32_16x16x32_f16 v[62:65], v[42:45], v[54:57], v[62:65]
	s_waitcnt lgkmcnt(7)
	v_mfma_f32_16x16x32_f16 v[66:69], v[42:45], v[94:97], v[66:69]
	s_waitcnt lgkmcnt(6)
	v_mfma_f32_16x16x32_f16 v[30:33], v[42:45], v[98:101], v[30:33]
	v_mfma_f32_16x16x32_f16 v[38:41], v[46:49], v[50:53], v[38:41]
	v_mfma_f32_16x16x32_f16 v[22:25], v[46:49], v[54:57], v[22:25]
	v_mfma_f32_16x16x32_f16 v[26:29], v[46:49], v[94:97], v[26:29]
	v_mfma_f32_16x16x32_f16 v[34:37], v[46:49], v[98:101], v[34:37]
	s_mov_b64 s[0:1], 0x22700
	v_lshl_add_u64 v[42:43], v[4:5], 0, s[0:1]
	s_mov_b32 s4, m0
	s_mov_b32 m0, s7
	s_nop 0
	global_load_lds_dwordx4 v[42:43], off
	s_mov_b32 m0, s4
	v_lshl_add_u64 v[42:43], v[6:7], 0, s[0:1]
	s_mov_b32 s0, m0
	s_mov_b32 m0, s15
	s_nop 0
	global_load_lds_dwordx4 v[42:43], off
	s_mov_b32 m0, s0
	ds_read_b128 v[42:45], v12
	ds_read_b128 v[46:49], v12 offset:2048
	ds_read_b128 v[50:53], v11 offset:16384
	ds_read_b128 v[54:57], v11 offset:18432
	ds_read_b128 v[94:97], v11 offset:20480
	ds_read_b128 v[98:101], v11 offset:22528
	s_waitcnt lgkmcnt(9)
	v_mfma_f32_16x16x32_f16 v[58:61], v[70:73], v[78:81], v[58:61]
	s_waitcnt lgkmcnt(8)
	v_mfma_f32_16x16x32_f16 v[62:65], v[70:73], v[82:85], v[62:65]
	s_waitcnt lgkmcnt(7)
	v_mfma_f32_16x16x32_f16 v[66:69], v[70:73], v[86:89], v[66:69]
	s_waitcnt lgkmcnt(6)
	v_mfma_f32_16x16x32_f16 v[30:33], v[70:73], v[90:93], v[30:33]
	v_mfma_f32_16x16x32_f16 v[38:41], v[74:77], v[78:81], v[38:41]
	v_mfma_f32_16x16x32_f16 v[22:25], v[74:77], v[82:85], v[22:25]
	v_mfma_f32_16x16x32_f16 v[26:29], v[74:77], v[86:89], v[26:29]
	v_mfma_f32_16x16x32_f16 v[34:37], v[74:77], v[90:93], v[34:37]
	s_mov_b64 s[0:1], 0x780
	s_waitcnt vmcnt(4)
	s_barrier
	v_lshl_add_u64 v[70:71], v[4:5], 0, s[0:1]
	s_mov_b32 s4, m0
	s_mov_b32 m0, s17
	s_nop 0
	global_load_lds_dwordx4 v[70:71], off
	s_mov_b32 m0, s4
	v_lshl_add_u64 v[70:71], v[6:7], 0, s[0:1]
	s_mov_b32 s0, m0
	s_mov_b32 m0, s19
	s_nop 0
	global_load_lds_dwordx4 v[70:71], off
	s_mov_b32 m0, s0
	ds_read_b128 v[70:73], v2 offset:32768
	ds_read_b128 v[74:77], v2 offset:34816
	ds_read_b128 v[78:81], v10 offset:49152
	ds_read_b128 v[82:85], v10 offset:51200
	ds_read_b128 v[86:89], v10 offset:53248
	ds_read_b128 v[90:93], v10 offset:55296
	s_waitcnt lgkmcnt(9)
	v_mfma_f32_16x16x32_f16 v[58:61], v[42:45], v[50:53], v[58:61]
	s_waitcnt lgkmcnt(8)
	v_mfma_f32_16x16x32_f16 v[62:65], v[42:45], v[54:57], v[62:65]
	s_waitcnt lgkmcnt(7)
	v_mfma_f32_16x16x32_f16 v[66:69], v[42:45], v[94:97], v[66:69]
	s_waitcnt lgkmcnt(6)
	v_mfma_f32_16x16x32_f16 v[30:33], v[42:45], v[98:101], v[30:33]
	v_mfma_f32_16x16x32_f16 v[38:41], v[46:49], v[50:53], v[38:41]
	v_mfma_f32_16x16x32_f16 v[22:25], v[46:49], v[54:57], v[22:25]
	v_mfma_f32_16x16x32_f16 v[26:29], v[46:49], v[94:97], v[26:29]
	v_mfma_f32_16x16x32_f16 v[34:37], v[46:49], v[98:101], v[34:37]
	s_mov_b64 s[0:1], 0x22780
	v_lshl_add_u64 v[4:5], v[4:5], 0, s[0:1]
	s_mov_b32 s4, m0
	s_mov_b32 m0, s2
	s_nop 0
	global_load_lds_dwordx4 v[4:5], off
	s_mov_b32 m0, s4
	v_lshl_add_u64 v[4:5], v[6:7], 0, s[0:1]
	s_mov_b32 s0, m0
	s_mov_b32 m0, s3
	s_nop 0
	global_load_lds_dwordx4 v[4:5], off
	s_mov_b32 m0, s0
	ds_read_b128 v[4:7], v12 offset:32768
	ds_read_b128 v[42:45], v12 offset:34816
	ds_read_b128 v[46:49], v11 offset:49152
	ds_read_b128 v[50:53], v11 offset:51200
	ds_read_b128 v[54:57], v11 offset:53248
	ds_read_b128 v[94:97], v11 offset:55296
	s_waitcnt lgkmcnt(9)
	v_mfma_f32_16x16x32_f16 v[58:61], v[70:73], v[78:81], v[58:61]
	s_waitcnt lgkmcnt(8)
	v_mfma_f32_16x16x32_f16 v[62:65], v[70:73], v[82:85], v[62:65]
	s_waitcnt lgkmcnt(7)
	v_mfma_f32_16x16x32_f16 v[66:69], v[70:73], v[86:89], v[66:69]
	s_waitcnt lgkmcnt(6)
	v_mfma_f32_16x16x32_f16 v[30:33], v[70:73], v[90:93], v[30:33]
	v_mfma_f32_16x16x32_f16 v[38:41], v[74:77], v[78:81], v[38:41]
	v_mfma_f32_16x16x32_f16 v[22:25], v[74:77], v[82:85], v[22:25]
	v_mfma_f32_16x16x32_f16 v[26:29], v[74:77], v[86:89], v[26:29]
	v_mfma_f32_16x16x32_f16 v[34:37], v[74:77], v[90:93], v[34:37]
	s_waitcnt vmcnt(4)
	s_barrier
	ds_read_b128 v[70:73], v14
	ds_read_b128 v[74:77], v14 offset:2048
	ds_read_b128 v[78:81], v13 offset:6144
	ds_read_b128 v[82:85], v13 offset:4096
	ds_read_b128 v[86:89], v13 offset:2048
	ds_read_b128 v[10:13], v13
	s_waitcnt lgkmcnt(9)
	v_mfma_f32_16x16x32_f16 v[58:61], v[4:7], v[46:49], v[58:61]
	s_waitcnt lgkmcnt(8)
	v_mfma_f32_16x16x32_f16 v[62:65], v[4:7], v[50:53], v[62:65]
	s_waitcnt lgkmcnt(7)
	v_mfma_f32_16x16x32_f16 v[66:69], v[4:7], v[54:57], v[66:69]
	s_waitcnt lgkmcnt(6)
	v_mfma_f32_16x16x32_f16 v[4:7], v[4:7], v[94:97], v[30:33]
	v_mfma_f32_16x16x32_f16 v[30:33], v[42:45], v[46:49], v[38:41]
	v_mfma_f32_16x16x32_f16 v[22:25], v[42:45], v[50:53], v[22:25]
	v_mfma_f32_16x16x32_f16 v[26:29], v[42:45], v[54:57], v[26:29]
	v_mfma_f32_16x16x32_f16 v[34:37], v[42:45], v[94:97], v[34:37]
	ds_read_b128 v[38:41], v16
	ds_read_b128 v[42:45], v16 offset:2048
	ds_read_b128 v[46:49], v15
	ds_read_b128 v[50:53], v15 offset:2048
	ds_read_b128 v[54:57], v15 offset:4096
	ds_read_b128 v[90:93], v15 offset:6144
	s_waitcnt lgkmcnt(6)
	v_mfma_f32_16x16x32_f16 v[58:61], v[70:73], v[10:13], v[58:61]
	v_mfma_f32_16x16x32_f16 v[62:65], v[70:73], v[86:89], v[62:65]
	v_mfma_f32_16x16x32_f16 v[66:69], v[70:73], v[82:85], v[66:69]
	v_mfma_f32_16x16x32_f16 v[4:7], v[70:73], v[78:81], v[4:7]
	v_mfma_f32_16x16x32_f16 v[10:13], v[74:77], v[10:13], v[30:33]
	v_mfma_f32_16x16x32_f16 v[22:25], v[74:77], v[86:89], v[22:25]
	v_mfma_f32_16x16x32_f16 v[26:29], v[74:77], v[82:85], v[26:29]
	v_mfma_f32_16x16x32_f16 v[30:33], v[74:77], v[78:81], v[34:37]
	s_waitcnt vmcnt(0)
	s_barrier
	s_nop 1
	ds_read_b128 v[34:37], v18 offset:6144
	ds_read_b128 v[70:73], v18 offset:4096
	ds_read_b128 v[74:77], v18 offset:2048
	ds_read_b128 v[78:81], v18
	ds_read_b128 v[82:85], v17 offset:2048
	ds_read_b128 v[14:17], v17
	s_waitcnt lgkmcnt(9)
	v_mfma_f32_16x16x32_f16 v[58:61], v[38:41], v[46:49], v[58:61]
	s_waitcnt lgkmcnt(8)
	v_mfma_f32_16x16x32_f16 v[62:65], v[38:41], v[50:53], v[62:65]
	s_waitcnt lgkmcnt(7)
	v_mfma_f32_16x16x32_f16 v[66:69], v[38:41], v[54:57], v[66:69]
	s_waitcnt lgkmcnt(6)
	v_mfma_f32_16x16x32_f16 v[4:7], v[38:41], v[90:93], v[4:7]
	v_mfma_f32_16x16x32_f16 v[10:13], v[42:45], v[46:49], v[10:13]
	v_mfma_f32_16x16x32_f16 v[22:25], v[42:45], v[50:53], v[22:25]
	v_mfma_f32_16x16x32_f16 v[26:29], v[42:45], v[54:57], v[26:29]
	v_mfma_f32_16x16x32_f16 v[30:33], v[42:45], v[90:93], v[30:33]
	ds_read_b128 v[38:41], v20
	ds_read_b128 v[42:45], v20 offset:2048
	ds_read_b128 v[46:49], v20 offset:4096
	ds_read_b128 v[50:53], v20 offset:6144
	ds_read_b128 v[54:57], v19 offset:2048
	ds_read_b128 v[18:21], v19
	v_and_b32_e32 v0, 64, v0
	s_waitcnt lgkmcnt(6)
	v_mfma_f32_16x16x32_f16 v[58:61], v[14:17], v[78:81], v[58:61]
	v_mfma_f32_16x16x32_f16 v[62:65], v[14:17], v[74:77], v[62:65]
	v_mfma_f32_16x16x32_f16 v[66:69], v[14:17], v[70:73], v[66:69]
	v_mfma_f32_16x16x32_f16 v[4:7], v[14:17], v[34:37], v[4:7]
	v_mfma_f32_16x16x32_f16 v[10:13], v[82:85], v[78:81], v[10:13]
	v_mfma_f32_16x16x32_f16 v[14:17], v[82:85], v[74:77], v[22:25]
	v_mfma_f32_16x16x32_f16 v[22:25], v[82:85], v[70:73], v[26:29]
	v_mfma_f32_16x16x32_f16 v[26:29], v[82:85], v[34:37], v[30:33]
	s_waitcnt lgkmcnt(0)
	v_mfma_f32_16x16x32_f16 v[30:33], v[18:21], v[38:41], v[58:61]
	v_mfma_f32_16x16x32_f16 v[34:37], v[18:21], v[42:45], v[62:65]
	v_mfma_f32_16x16x32_f16 v[58:61], v[18:21], v[46:49], v[66:69]
	v_mfma_f32_16x16x32_f16 v[4:7], v[18:21], v[50:53], v[4:7]
	v_mfma_f32_16x16x32_f16 v[10:13], v[54:57], v[38:41], v[10:13]
	v_mfma_f32_16x16x32_f16 v[14:17], v[54:57], v[42:45], v[14:17]
	v_mfma_f32_16x16x32_f16 v[18:21], v[54:57], v[46:49], v[22:25]
	v_mfma_f32_16x16x32_f16 v[22:25], v[54:57], v[50:53], v[26:29]
	s_lshl_b32 s0, s13, 7
	v_or3_b32 v0, s0, v0, v9
	v_lshlrev_b32_e32 v2, 2, v0
	global_load_dword v46, v2, s[8:9]
	global_load_dword v47, v2, s[8:9] offset:64
	global_load_dword v48, v2, s[8:9] offset:128
	global_load_dword v49, v2, s[8:9] offset:192
	v_and_b32_e32 v0, 12, v1
	v_or3_b32 v0, s12, v8, v0
	v_ashrrev_i32_e32 v1, 31, v0
	v_or_b32_e32 v8, 1, v0
	v_or_b32_e32 v26, 2, v0
	v_or_b32_e32 v28, 3, v0
	v_or_b32_e32 v38, 16, v0
	v_or_b32_e32 v40, 17, v0
	v_or_b32_e32 v42, 18, v0
	v_or_b32_e32 v44, 19, v0
	v_lshl_add_u64 v[2:3], s[10:11], 0, v[2:3]
	v_lshlrev_b64 v[0:1], 12, v[0:1]
	v_ashrrev_i32_e32 v9, 31, v8
	v_ashrrev_i32_e32 v27, 31, v26
	v_ashrrev_i32_e32 v29, 31, v28
	v_ashrrev_i32_e32 v39, 31, v38
	v_ashrrev_i32_e32 v41, 31, v40
	v_ashrrev_i32_e32 v43, 31, v42
	v_ashrrev_i32_e32 v45, 31, v44
	v_lshl_add_u64 v[0:1], v[2:3], 0, v[0:1]
	v_lshlrev_b64 v[8:9], 12, v[8:9]
	v_lshlrev_b64 v[26:27], 12, v[26:27]
	v_lshlrev_b64 v[28:29], 12, v[28:29]
	v_lshlrev_b64 v[38:39], 12, v[38:39]
	v_lshlrev_b64 v[40:41], 12, v[40:41]
	v_lshlrev_b64 v[42:43], 12, v[42:43]
	v_lshlrev_b64 v[44:45], 12, v[44:45]
	v_lshl_add_u64 v[8:9], v[2:3], 0, v[8:9]
	v_lshl_add_u64 v[26:27], v[2:3], 0, v[26:27]
	v_lshl_add_u64 v[28:29], v[2:3], 0, v[28:29]
	v_lshl_add_u64 v[38:39], v[2:3], 0, v[38:39]
	v_lshl_add_u64 v[40:41], v[2:3], 0, v[40:41]
	v_lshl_add_u64 v[42:43], v[2:3], 0, v[42:43]
	v_lshl_add_u64 v[2:3], v[2:3], 0, v[44:45]
	s_waitcnt vmcnt(3)
	v_add_f32_e32 v30, v46, v30
	v_add_f32_e32 v31, v46, v31
	v_add_f32_e32 v32, v46, v32
	s_waitcnt vmcnt(0)
	v_add_f32_e32 v4, v49, v4
	v_add_f32_e32 v33, v46, v33
	v_add_f32_e32 v10, v46, v10
	v_add_f32_e32 v11, v46, v11
	v_add_f32_e32 v12, v46, v12
	v_add_f32_e32 v13, v46, v13
	v_add_f32_e32 v34, v47, v34
	v_add_f32_e32 v35, v47, v35
	v_add_f32_e32 v36, v47, v36
	v_add_f32_e32 v37, v47, v37
	v_add_f32_e32 v14, v47, v14
	v_add_f32_e32 v15, v47, v15
	v_add_f32_e32 v16, v47, v16
	v_add_f32_e32 v17, v47, v17
	v_add_f32_e32 v44, v48, v58
	v_add_f32_e32 v45, v48, v59
	v_add_f32_e32 v46, v48, v60
	v_add_f32_e32 v47, v48, v61
	v_add_f32_e32 v18, v48, v18
	v_add_f32_e32 v19, v48, v19
	global_store_dword v[0:1], v30, off
	global_store_dword v[8:9], v31, off
	global_store_dword v[26:27], v32, off
	global_store_dword v[28:29], v33, off
	global_store_dword v[38:39], v10, off
	global_store_dword v[40:41], v11, off
	global_store_dword v[42:43], v12, off
	global_store_dword v[2:3], v13, off
	global_store_dword v[0:1], v34, off offset:64
	global_store_dword v[8:9], v35, off offset:64
	global_store_dword v[26:27], v36, off offset:64
	global_store_dword v[28:29], v37, off offset:64
	global_store_dword v[38:39], v14, off offset:64
	global_store_dword v[40:41], v15, off offset:64
	global_store_dword v[42:43], v16, off offset:64
	global_store_dword v[2:3], v17, off offset:64
	global_store_dword v[0:1], v44, off offset:128
	global_store_dword v[8:9], v45, off offset:128
	global_store_dword v[26:27], v46, off offset:128
	global_store_dword v[28:29], v47, off offset:128
	global_store_dword v[38:39], v18, off offset:128
	global_store_dword v[40:41], v19, off offset:128
	global_store_dword v[0:1], v4, off offset:192
	v_add_f32_e32 v0, v49, v5
	global_store_dword v[8:9], v0, off offset:192
	v_add_f32_e32 v0, v49, v6
	global_store_dword v[26:27], v0, off offset:192
	v_add_f32_e32 v0, v49, v7
	global_store_dword v[28:29], v0, off offset:192
	v_add_f32_e32 v0, v49, v22
	global_store_dword v[38:39], v0, off offset:192
	v_add_f32_e32 v0, v49, v23
	v_add_f32_e32 v10, v48, v20
	global_store_dword v[40:41], v0, off offset:192
	v_add_f32_e32 v0, v49, v24
	global_store_dword v[42:43], v10, off offset:128
	v_add_f32_e32 v10, v48, v21
	global_store_dword v[42:43], v0, off offset:192
	v_add_f32_e32 v0, v49, v25
	global_store_dword v[2:3], v10, off offset:128
	global_store_dword v[2:3], v0, off offset:192
	s_endpgm
